# v45 + router logit reductions (P10): all 48 ds_bpermute exchanges replaced by DPP moves / permlane swaps (bit-identical)
# baseline (speedup 1.0000x reference)
.LBB0_1696:
	s_or_b64 exec, exec, s[2:3]
	ds_read_b128 v[96:99], v88
	ds_read_b128 v[100:103], v88 offset:16
	ds_read_b128 v[104:107], v88 offset:32
	ds_read_b128 v[108:111], v88 offset:48
	s_waitcnt lgkmcnt(3)
	v_fma_f32 v95, v76, v98, 0
	v_fma_f32 v94, v76, v99, 0
	s_waitcnt lgkmcnt(2)
	v_fma_f32 v79, v76, v100, 0
	v_fma_f32 v78, v76, v101, 0
	s_waitcnt lgkmcnt(1)
	v_fmac_f32_e32 v95, v77, v106
	v_fmac_f32_e32 v94, v77, v107
	s_waitcnt lgkmcnt(0)
	v_fmac_f32_e32 v79, v77, v108
	ds_read_b128 v[98:101], v88 offset:64
	v_fmac_f32_e32 v78, v77, v109
	ds_read_b128 v[106:109], v88 offset:80
	v_fma_f32 v73, v76, v102, 0
	v_fma_f32 v72, v76, v103, 0
	v_fmac_f32_e32 v73, v77, v110
	v_fmac_f32_e32 v72, v77, v111
	s_waitcnt lgkmcnt(1)
	v_fmac_f32_e32 v95, v74, v100
	v_fmac_f32_e32 v94, v74, v101
	s_waitcnt lgkmcnt(0)
	v_fmac_f32_e32 v79, v74, v106
	v_fmac_f32_e32 v78, v74, v107
	v_fmac_f32_e32 v73, v74, v108
	v_fmac_f32_e32 v72, v74, v109
	ds_read_b128 v[100:103], v88 offset:96
	ds_read_b128 v[106:109], v88 offset:112
	v_pk_fma_f32 v[96:97], v[76:77], v[96:97], 0 op_sel_hi:[0,1,0]
	v_pk_fma_f32 v[76:77], v[76:77], v[104:105], v[96:97] op_sel:[1,0,0]
	ds_read_b128 v[112:115], v88 offset:16400
	v_pk_fma_f32 v[76:77], v[74:75], v[98:99], v[76:77] op_sel_hi:[0,1,1]
	v_mov_b32_e32 v74, v75
	s_waitcnt lgkmcnt(2)
	v_pk_fma_f32 v[130:131], v[74:75], v[100:101], v[76:77] op_sel_hi:[0,1,1]
	v_fmac_f32_e32 v95, v75, v102
	v_fmac_f32_e32 v94, v75, v103
	ds_read_b128 v[96:99], v88 offset:8192
	ds_read_b128 v[100:103], v88 offset:8208
	s_waitcnt lgkmcnt(3)
	v_fmac_f32_e32 v79, v75, v106
	v_fmac_f32_e32 v78, v75, v107
	v_fmac_f32_e32 v73, v75, v108
	v_fmac_f32_e32 v72, v75, v109
	s_waitcnt lgkmcnt(1)
	v_fmac_f32_e32 v95, v70, v98
	v_fmac_f32_e32 v94, v70, v99
	s_waitcnt lgkmcnt(0)
	v_fmac_f32_e32 v79, v70, v100
	ds_read_b128 v[74:77], v88 offset:8224
	v_fmac_f32_e32 v78, v70, v101
	ds_read_b128 v[98:101], v88 offset:8240
	v_fmac_f32_e32 v73, v70, v102
	v_fmac_f32_e32 v72, v70, v103
	ds_read_b128 v[102:105], v88 offset:8256
	ds_read_b128 v[106:109], v88 offset:8272
	s_waitcnt lgkmcnt(3)
	v_fmac_f32_e32 v95, v71, v76
	v_fmac_f32_e32 v94, v71, v77
	s_waitcnt lgkmcnt(2)
	v_fmac_f32_e32 v79, v71, v98
	v_fmac_f32_e32 v78, v71, v99
	v_fmac_f32_e32 v73, v71, v100
	v_fmac_f32_e32 v72, v71, v101
	s_waitcnt lgkmcnt(1)
	v_fmac_f32_e32 v95, v66, v104
	v_fmac_f32_e32 v94, v66, v105
	s_waitcnt lgkmcnt(0)
	v_fmac_f32_e32 v79, v66, v106
	ds_read_b128 v[98:101], v88 offset:8288
	v_fmac_f32_e32 v78, v66, v107
	ds_read_b128 v[104:107], v88 offset:8304
	v_fmac_f32_e32 v73, v66, v108
	v_fmac_f32_e32 v72, v66, v109
	ds_read_b128 v[108:111], v88 offset:16384
	s_waitcnt lgkmcnt(2)
	v_fmac_f32_e32 v95, v67, v100
	v_fmac_f32_e32 v94, v67, v101
	s_waitcnt lgkmcnt(1)
	v_fmac_f32_e32 v79, v67, v104
	v_fmac_f32_e32 v78, v67, v105
	v_fmac_f32_e32 v73, v67, v106
	v_fmac_f32_e32 v72, v67, v107
	s_waitcnt lgkmcnt(0)
	v_fmac_f32_e32 v95, v68, v110
	v_fmac_f32_e32 v94, v68, v111
	v_fmac_f32_e32 v79, v68, v112
	ds_read_b128 v[104:107], v88 offset:16416
	v_fmac_f32_e32 v78, v68, v113
	ds_read_b128 v[110:113], v88 offset:16432
	v_fmac_f32_e32 v73, v68, v114
	v_fmac_f32_e32 v72, v68, v115
	ds_read_b128 v[114:117], v88 offset:16448
	ds_read_b128 v[118:121], v88 offset:16464
	s_waitcnt lgkmcnt(3)
	v_fmac_f32_e32 v95, v69, v106
	v_fmac_f32_e32 v94, v69, v107
	s_waitcnt lgkmcnt(2)
	v_fmac_f32_e32 v79, v69, v110
	v_fmac_f32_e32 v78, v69, v111
	v_fmac_f32_e32 v73, v69, v112
	v_fmac_f32_e32 v72, v69, v113
	s_waitcnt lgkmcnt(1)
	v_fmac_f32_e32 v95, v62, v116
	v_fmac_f32_e32 v94, v62, v117
	s_waitcnt lgkmcnt(0)
	v_fmac_f32_e32 v79, v62, v118
	ds_read_b128 v[110:113], v88 offset:16480
	v_fmac_f32_e32 v78, v62, v119
	ds_read_b128 v[116:119], v88 offset:16496
	v_fmac_f32_e32 v73, v62, v120
	v_fmac_f32_e32 v72, v62, v121
	ds_read_b128 v[120:123], v88 offset:24576
	ds_read_b128 v[124:127], v88 offset:24592
	s_waitcnt lgkmcnt(3)
	v_fmac_f32_e32 v95, v63, v112
	v_fmac_f32_e32 v94, v63, v113
	s_waitcnt lgkmcnt(2)
	v_fmac_f32_e32 v79, v63, v116
	v_fmac_f32_e32 v78, v63, v117
	v_pk_fma_f32 v[76:77], v[70:71], v[96:97], v[130:131] op_sel_hi:[0,1,1]
	v_fmac_f32_e32 v73, v63, v118
	v_fmac_f32_e32 v72, v63, v119
	s_waitcnt lgkmcnt(1)
	v_fmac_f32_e32 v95, v64, v122
	v_fmac_f32_e32 v94, v64, v123
	s_waitcnt lgkmcnt(0)
	v_fmac_f32_e32 v79, v64, v124
	ds_read_b128 v[116:119], v88 offset:24608
	v_fmac_f32_e32 v78, v64, v125
	ds_read_b128 v[122:125], v88 offset:24624
	v_pk_fma_f32 v[70:71], v[70:71], v[74:75], v[76:77] op_sel:[1,0,0]
	v_fmac_f32_e32 v73, v64, v126
	v_pk_fma_f32 v[70:71], v[66:67], v[102:103], v[70:71] op_sel_hi:[0,1,1]
	v_mov_b32_e32 v66, v67
	v_pk_fma_f32 v[66:67], v[66:67], v[98:99], v[70:71] op_sel_hi:[0,1,1]
	v_pk_fma_f32 v[66:67], v[68:69], v[108:109], v[66:67] op_sel_hi:[0,1,1]
	v_fmac_f32_e32 v72, v64, v127
	v_pk_fma_f32 v[66:67], v[68:69], v[104:105], v[66:67] op_sel:[1,0,0]
	s_waitcnt lgkmcnt(0)
	v_fmac_f32_e32 v79, v65, v122
	v_fmac_f32_e32 v78, v65, v123
	v_fmac_f32_e32 v73, v65, v124
	v_fmac_f32_e32 v72, v65, v125
	ds_read_b128 v[122:125], v88 offset:24640
	ds_read_b128 v[126:129], v88 offset:24656
	v_pk_fma_f32 v[66:67], v[62:63], v[114:115], v[66:67] op_sel_hi:[0,1,1]
	v_mov_b32_e32 v62, v63
	v_pk_fma_f32 v[62:63], v[62:63], v[110:111], v[66:67] op_sel_hi:[0,1,1]
	v_pk_fma_f32 v[62:63], v[64:65], v[120:121], v[62:63] op_sel_hi:[0,1,1]
	v_pk_fma_f32 v[62:63], v[64:65], v[116:117], v[62:63] op_sel:[1,0,0]
	v_fmac_f32_e32 v95, v65, v118
	v_fmac_f32_e32 v94, v65, v119
	s_waitcnt lgkmcnt(1)
	v_pk_fma_f32 v[118:119], v[60:61], v[122:123], v[62:63] op_sel_hi:[0,1,1]
	ds_read_b128 v[62:65], v88 offset:24672
	ds_read_b128 v[66:69], v88 offset:24688
	v_fmac_f32_e32 v95, v60, v124
	v_fmac_f32_e32 v94, v60, v125
	s_waitcnt lgkmcnt(2)
	v_fmac_f32_e32 v79, v60, v126
	v_fmac_f32_e32 v78, v60, v127
	v_fmac_f32_e32 v73, v60, v128
	v_fmac_f32_e32 v72, v60, v129
	s_waitcnt lgkmcnt(1)
	v_fmac_f32_e32 v95, v61, v64
	v_fmac_f32_e32 v94, v61, v65
	s_waitcnt lgkmcnt(0)
	v_fmac_f32_e32 v79, v61, v66
	ds_read_b128 v[74:77], v88 offset:32768
	v_fmac_f32_e32 v78, v61, v67
	ds_read_b128 v[64:67], v88 offset:32784
	v_fmac_f32_e32 v73, v61, v68
	v_fmac_f32_e32 v72, v61, v69
	ds_read_b128 v[68:71], v88 offset:32800
	ds_read_b128 v[96:99], v88 offset:32816
	s_waitcnt lgkmcnt(2)
	v_fmac_f32_e32 v79, v58, v64
	v_fmac_f32_e32 v78, v58, v65
	v_fmac_f32_e32 v73, v58, v66
	v_fmac_f32_e32 v72, v58, v67
	ds_read_b128 v[64:67], v88 offset:32832
	ds_read_b128 v[100:103], v88 offset:32848
	s_waitcnt lgkmcnt(2)
	v_fmac_f32_e32 v79, v59, v96
	v_fmac_f32_e32 v78, v59, v97
	v_fmac_f32_e32 v73, v59, v98
	v_fmac_f32_e32 v72, v59, v99
	ds_read_b128 v[96:99], v88 offset:32864
	ds_read_b128 v[104:107], v88 offset:32880
	v_fmac_f32_e32 v95, v58, v76
	v_fmac_f32_e32 v94, v58, v77
	v_fmac_f32_e32 v95, v59, v70
	v_fmac_f32_e32 v94, v59, v71
	s_waitcnt lgkmcnt(3)
	v_fmac_f32_e32 v95, v54, v66
	v_fmac_f32_e32 v94, v54, v67
	s_waitcnt lgkmcnt(2)
	v_fmac_f32_e32 v79, v54, v100
	v_fmac_f32_e32 v78, v54, v101
	v_fmac_f32_e32 v73, v54, v102
	v_fmac_f32_e32 v72, v54, v103
	s_waitcnt lgkmcnt(1)
	v_fmac_f32_e32 v95, v55, v98
	v_fmac_f32_e32 v94, v55, v99
	s_waitcnt lgkmcnt(0)
	v_fmac_f32_e32 v79, v55, v104
	ds_read_b128 v[98:101], v88 offset:40960
	v_fmac_f32_e32 v78, v55, v105
	ds_read_b128 v[102:105], v88 offset:40976
	v_fmac_f32_e32 v73, v55, v106
	v_fmac_f32_e32 v72, v55, v107
	ds_read_b128 v[106:109], v88 offset:40992
	s_waitcnt lgkmcnt(2)
	v_fmac_f32_e32 v95, v56, v100
	v_fmac_f32_e32 v94, v56, v101
	s_waitcnt lgkmcnt(1)
	v_fmac_f32_e32 v79, v56, v102
	v_fmac_f32_e32 v78, v56, v103
	ds_read_b128 v[100:103], v88 offset:41008
	v_fmac_f32_e32 v73, v56, v104
	v_fmac_f32_e32 v72, v56, v105
	s_waitcnt lgkmcnt(1)
	v_fmac_f32_e32 v95, v57, v108
	v_fmac_f32_e32 v94, v57, v109
	ds_read_b128 v[108:111], v88 offset:41024
	ds_read_b128 v[112:115], v88 offset:41040
	s_waitcnt lgkmcnt(2)
	v_fmac_f32_e32 v79, v57, v100
	v_fmac_f32_e32 v78, v57, v101
	v_fmac_f32_e32 v73, v57, v102
	v_fmac_f32_e32 v72, v57, v103
	ds_read_b128 v[100:103], v88 offset:41056
	v_mov_b32_e32 v60, v61
	s_waitcnt lgkmcnt(2)
	v_fmac_f32_e32 v95, v52, v110
	v_fmac_f32_e32 v94, v52, v111
	s_waitcnt lgkmcnt(1)
	v_fmac_f32_e32 v79, v52, v112
	v_fmac_f32_e32 v78, v52, v113
	ds_read_b128 v[110:113], v88 offset:41072
	v_pk_fma_f32 v[60:61], v[60:61], v[62:63], v[118:119] op_sel_hi:[0,1,1]
	v_fmac_f32_e32 v73, v52, v114
	v_fmac_f32_e32 v72, v52, v115
	s_waitcnt lgkmcnt(1)
	v_fmac_f32_e32 v95, v53, v102
	v_fmac_f32_e32 v94, v53, v103
	ds_read_b128 v[102:105], v88 offset:49152
	ds_read_b128 v[114:117], v88 offset:49168
	v_pk_fma_f32 v[60:61], v[58:59], v[74:75], v[60:61] op_sel_hi:[0,1,1]
	v_pk_fma_f32 v[58:59], v[58:59], v[68:69], v[60:61] op_sel:[1,0,0]
	s_waitcnt lgkmcnt(2)
	v_fmac_f32_e32 v79, v53, v110
	v_pk_fma_f32 v[58:59], v[54:55], v[64:65], v[58:59] op_sel_hi:[0,1,1]
	v_mov_b32_e32 v54, v55
	v_pk_fma_f32 v[54:55], v[54:55], v[96:97], v[58:59] op_sel_hi:[0,1,1]
	v_fmac_f32_e32 v78, v53, v111
	v_fmac_f32_e32 v73, v53, v112
	v_fmac_f32_e32 v72, v53, v113
	v_pk_fma_f32 v[54:55], v[56:57], v[98:99], v[54:55] op_sel_hi:[0,1,1]
	s_waitcnt lgkmcnt(0)
	v_fmac_f32_e32 v79, v50, v114
	v_fmac_f32_e32 v78, v50, v115
	v_fmac_f32_e32 v73, v50, v116
	v_fmac_f32_e32 v72, v50, v117
	ds_read_b128 v[110:113], v88 offset:49184
	ds_read_b128 v[114:117], v88 offset:49200
	v_pk_fma_f32 v[54:55], v[56:57], v[106:107], v[54:55] op_sel:[1,0,0]
	ds_read_b128 v[56:59], v88 offset:49232
	v_pk_fma_f32 v[54:55], v[52:53], v[108:109], v[54:55] op_sel_hi:[0,1,1]
	v_mov_b32_e32 v52, v53
	v_pk_fma_f32 v[52:53], v[52:53], v[100:101], v[54:55] op_sel_hi:[0,1,1]
	v_pk_fma_f32 v[52:53], v[50:51], v[102:103], v[52:53] op_sel_hi:[0,1,1]
	s_waitcnt lgkmcnt(2)
	v_pk_fma_f32 v[100:101], v[50:51], v[110:111], v[52:53] op_sel:[1,0,0]
	ds_read_b128 v[52:55], v88 offset:49216
	v_fmac_f32_e32 v95, v50, v104
	v_fmac_f32_e32 v94, v50, v105
	v_fmac_f32_e32 v95, v51, v112
	v_fmac_f32_e32 v94, v51, v113
	s_waitcnt lgkmcnt(2)
	v_fmac_f32_e32 v79, v51, v114
	v_fmac_f32_e32 v78, v51, v115
	ds_read_b128 v[60:63], v88 offset:49248
	s_waitcnt lgkmcnt(1)
	v_fmac_f32_e32 v95, v46, v54
	v_fmac_f32_e32 v94, v46, v55
	v_fmac_f32_e32 v79, v46, v56
	v_fmac_f32_e32 v78, v46, v57
	ds_read_b128 v[54:57], v88 offset:49264
	v_fmac_f32_e32 v73, v51, v116
	v_fmac_f32_e32 v72, v51, v117
	v_fmac_f32_e32 v73, v46, v58
	v_fmac_f32_e32 v72, v46, v59
	s_waitcnt lgkmcnt(1)
	v_fmac_f32_e32 v95, v47, v62
	v_fmac_f32_e32 v94, v47, v63
	ds_read_b128 v[62:65], v88 offset:57344
	ds_read_b128 v[66:69], v88 offset:57360
	s_waitcnt lgkmcnt(2)
	v_fmac_f32_e32 v79, v47, v54
	v_fmac_f32_e32 v78, v47, v55
	v_fmac_f32_e32 v73, v47, v56
	v_fmac_f32_e32 v72, v47, v57
	ds_read_b128 v[54:57], v88 offset:57376
	s_waitcnt lgkmcnt(2)
	v_fmac_f32_e32 v95, v48, v64
	v_fmac_f32_e32 v94, v48, v65
	v_pk_fma_f32 v[50:51], v[46:47], v[52:53], v[100:101] op_sel_hi:[0,1,1]
	v_mov_b32_e32 v46, v47
	s_waitcnt lgkmcnt(1)
	v_fmac_f32_e32 v79, v48, v66
	v_fmac_f32_e32 v78, v48, v67
	ds_read_b128 v[64:67], v88 offset:57392
	v_fmac_f32_e32 v73, v48, v68
	v_fmac_f32_e32 v72, v48, v69
	s_waitcnt lgkmcnt(1)
	v_fmac_f32_e32 v95, v49, v56
	v_fmac_f32_e32 v94, v49, v57
	ds_read_b128 v[56:59], v88 offset:57408
	ds_read_b128 v[68:71], v88 offset:57424
	ds_read_b128 v[74:77], v88 offset:57440
	ds_read_b128 v[96:99], v88 offset:57456
	v_pk_fma_f32 v[46:47], v[46:47], v[60:61], v[50:51] op_sel_hi:[0,1,1]
	v_pk_fma_f32 v[46:47], v[48:49], v[62:63], v[46:47] op_sel_hi:[0,1,1]
	v_pk_fma_f32 v[46:47], v[48:49], v[54:55], v[46:47] op_sel:[1,0,0]
	v_mov_b32_e32 v48, v45
	s_waitcnt lgkmcnt(3)
	v_pk_fma_f32 v[46:47], v[44:45], v[56:57], v[46:47] op_sel_hi:[0,1,1]
	s_waitcnt lgkmcnt(1)
	v_pk_fma_f32 v[46:47], v[48:49], v[74:75], v[46:47] op_sel_hi:[0,1,1]
	s_nop 1
	v_mov_b32_dpp v50, v46 quad_perm:[1,0,3,2] row_mask:0xf bank_mask:0xf
	s_nop 1
	v_mov_b32_dpp v51, v47 quad_perm:[1,0,3,2] row_mask:0xf bank_mask:0xf
	v_fmac_f32_e32 v79, v49, v64
	v_fmac_f32_e32 v78, v49, v65
	v_fmac_f32_e32 v73, v49, v66
	v_fmac_f32_e32 v72, v49, v67
	s_waitcnt lgkmcnt(0)
	v_pk_add_f32 v[46:47], v[46:47], v[50:51]
	s_nop 1
	v_mov_b32_dpp v48, v46 quad_perm:[2,3,0,1] row_mask:0xf bank_mask:0xf
	s_nop 1
	v_mov_b32_dpp v49, v47 quad_perm:[2,3,0,1] row_mask:0xf bank_mask:0xf
	v_fmac_f32_e32 v95, v44, v58
	v_fmac_f32_e32 v95, v45, v76
	v_fmac_f32_e32 v94, v44, v59
	v_fmac_f32_e32 v79, v44, v68
	s_waitcnt lgkmcnt(0)
	v_pk_add_f32 v[46:47], v[46:47], v[48:49]
	v_fmac_f32_e32 v78, v44, v69
	v_fmac_f32_e32 v73, v44, v70
	v_fmac_f32_e32 v72, v44, v71
	s_nop 1
	v_mov_b32_dpp v48, v46 row_half_mirror row_mask:0xf bank_mask:0xf
	s_nop 1
	v_mov_b32_dpp v49, v47 row_half_mirror row_mask:0xf bank_mask:0xf
	s_nop 1
	v_mov_b32_dpp v44, v95 quad_perm:[1,0,3,2] row_mask:0xf bank_mask:0xf
	v_fmac_f32_e32 v94, v45, v77
	v_fmac_f32_e32 v79, v45, v96
	v_fmac_f32_e32 v78, v45, v97
	s_waitcnt lgkmcnt(1)
	v_pk_add_f32 v[46:47], v[46:47], v[48:49]
	s_waitcnt lgkmcnt(0)
	v_add_f32_e32 v50, v95, v44
	s_nop 1
	v_mov_b32_dpp v48, v46 row_mirror row_mask:0xf bank_mask:0xf
	s_nop 1
	v_mov_b32_dpp v49, v47 row_mirror row_mask:0xf bank_mask:0xf
	s_nop 1
	v_mov_b32_dpp v51, v50 quad_perm:[2,3,0,1] row_mask:0xf bank_mask:0xf
	v_fmac_f32_e32 v73, v45, v98
	v_fmac_f32_e32 v72, v45, v99
	s_nop 1
	v_mov_b32_dpp v55, v78 quad_perm:[1,0,3,2] row_mask:0xf bank_mask:0xf
	s_waitcnt lgkmcnt(2)
	v_pk_add_f32 v[44:45], v[46:47], v[48:49]
	s_waitcnt lgkmcnt(1)
	v_add_f32_e32 v49, v50, v51
	v_mov_b32_e32 v46, v44
	s_nop 1
	v_permlane16_swap_b32_e32 v46, v44
	v_mov_b32_e32 v47, v45
	s_nop 1
	v_permlane16_swap_b32_e32 v47, v45
	s_nop 1
	v_mov_b32_dpp v48, v94 quad_perm:[1,0,3,2] row_mask:0xf bank_mask:0xf
	s_nop 1
	v_mov_b32_dpp v50, v49 row_half_mirror row_mask:0xf bank_mask:0xf
	s_nop 1
	v_mov_b32_dpp v51, v79 quad_perm:[1,0,3,2] row_mask:0xf bank_mask:0xf
	s_nop 1
	v_mov_b32_dpp v56, v72 quad_perm:[1,0,3,2] row_mask:0xf bank_mask:0xf
	s_waitcnt lgkmcnt(4)
	v_pk_add_f32 v[44:45], v[44:45], v[46:47]
	s_waitcnt lgkmcnt(3)
	v_add_f32_e32 v46, v94, v48
	s_waitcnt lgkmcnt(2)
	v_add_f32_e32 v48, v49, v50
	s_waitcnt lgkmcnt(1)
	v_add_f32_e32 v49, v79, v51
	s_nop 1
	v_mov_b32_dpp v47, v46 quad_perm:[2,3,0,1] row_mask:0xf bank_mask:0xf
	s_nop 1
	v_mov_b32_dpp v50, v49 quad_perm:[2,3,0,1] row_mask:0xf bank_mask:0xf
	s_nop 1
	v_mov_b32_dpp v51, v48 row_mirror row_mask:0xf bank_mask:0xf
	v_add_f32_e32 v55, v78, v55
	s_waitcnt lgkmcnt(3)
	v_add_f32_e32 v56, v72, v56
	s_waitcnt lgkmcnt(2)
	v_add_f32_e32 v47, v46, v47
	s_waitcnt lgkmcnt(1)
	v_add_f32_e32 v49, v49, v50
	s_nop 1
	v_mov_b32_dpp v52, v47 row_half_mirror row_mask:0xf bank_mask:0xf
	s_nop 1
	v_mov_b32_dpp v50, v49 row_half_mirror row_mask:0xf bank_mask:0xf
	s_waitcnt lgkmcnt(2)
	v_add_f32_e32 v48, v48, v51
	v_mov_b32_e32 v53, v48
	s_nop 1
	v_permlane16_swap_b32_e32 v53, v48
	s_nop 1
	v_mov_b32_dpp v57, v55 quad_perm:[2,3,0,1] row_mask:0xf bank_mask:0xf
	s_waitcnt lgkmcnt(3)
	v_add_f32_e32 v51, v47, v52
	s_waitcnt lgkmcnt(2)
	v_add_f32_e32 v49, v49, v50
	s_nop 1
	v_mov_b32_dpp v52, v51 row_mirror row_mask:0xf bank_mask:0xf
	s_nop 1
	v_mov_b32_dpp v50, v49 row_mirror row_mask:0xf bank_mask:0xf
	s_waitcnt lgkmcnt(3)
	v_add_f32_e32 v48, v48, v53
	s_nop 1
	v_mov_b32_dpp v59, v56 quad_perm:[2,3,0,1] row_mask:0xf bank_mask:0xf
	s_waitcnt lgkmcnt(3)
	v_add_f32_e32 v55, v55, v57
	s_waitcnt lgkmcnt(2)
	v_add_f32_e32 v51, v51, v52
	s_waitcnt lgkmcnt(1)
	v_add_f32_e32 v53, v49, v50
	v_mov_b32_e32 v52, v51
	s_nop 1
	v_permlane16_swap_b32_e32 v52, v51
	v_mov_b32_e32 v54, v53
	s_nop 1
	v_permlane16_swap_b32_e32 v54, v53
	s_waitcnt lgkmcnt(2)
	v_add_f32_e32 v56, v56, v59
	s_nop 1
	v_mov_b32_dpp v57, v55 row_half_mirror row_mask:0xf bank_mask:0xf
	s_nop 1
	v_mov_b32_dpp v59, v56 row_half_mirror row_mask:0xf bank_mask:0xf
	s_waitcnt lgkmcnt(3)
	v_add_f32_e32 v50, v51, v52
	s_waitcnt lgkmcnt(2)
	v_add_f32_e32 v52, v53, v54
	s_nop 1
	v_mov_b32_dpp v54, v73 quad_perm:[1,0,3,2] row_mask:0xf bank_mask:0xf
	s_waitcnt lgkmcnt(2)
	v_add_f32_e32 v55, v55, v57
	s_waitcnt lgkmcnt(1)
	v_add_f32_e32 v56, v56, v59
	s_nop 1
	v_mov_b32_dpp v57, v55 row_mirror row_mask:0xf bank_mask:0xf
	s_nop 1
	v_mov_b32_dpp v59, v56 row_mirror row_mask:0xf bank_mask:0xf
	s_waitcnt lgkmcnt(2)
	v_add_f32_e32 v54, v73, v54
	s_nop 1
	v_mov_b32_dpp v58, v54 quad_perm:[2,3,0,1] row_mask:0xf bank_mask:0xf
	v_mov_b32_e32 v46, v44
	s_nop 1
	v_permlane32_swap_b32_e32 v46, v44
	s_waitcnt lgkmcnt(3)
	v_add_f32_e32 v55, v55, v57
	s_waitcnt lgkmcnt(2)
	v_add_f32_e32 v59, v56, v59
	v_mov_b32_e32 v57, v55
	s_nop 1
	v_permlane16_swap_b32_e32 v57, v55
	s_waitcnt lgkmcnt(2)
	v_add_f32_e32 v54, v54, v58
	s_nop 1
	v_mov_b32_dpp v58, v54 row_half_mirror row_mask:0xf bank_mask:0xf
	v_mov_b32_e32 v61, v59
	s_nop 1
	v_permlane16_swap_b32_e32 v61, v59
	v_mov_b32_e32 v47, v45
	s_nop 1
	v_permlane32_swap_b32_e32 v47, v45
	v_mov_b32_e32 v49, v48
	s_nop 1
	v_permlane32_swap_b32_e32 v49, v48
	v_mov_b32_e32 v51, v50
	s_nop 1
	v_permlane32_swap_b32_e32 v51, v50
	s_waitcnt lgkmcnt(4)
	v_add_f32_e32 v54, v54, v58
	s_nop 1
	v_mov_b32_dpp v58, v54 row_mirror row_mask:0xf bank_mask:0xf
	v_mov_b32_e32 v53, v52
	s_nop 1
	v_permlane32_swap_b32_e32 v53, v52
	s_waitcnt lgkmcnt(1)
	v_add_f32_e32 v58, v54, v58
	v_mov_b32_e32 v60, v58
	s_nop 1
	v_permlane16_swap_b32_e32 v60, v58
	v_add_f32_e32 v54, v55, v57
	v_mov_b32_e32 v55, v54
	s_nop 1
	v_permlane32_swap_b32_e32 v55, v54
	s_waitcnt lgkmcnt(1)
	v_add_f32_e32 v56, v58, v60
	v_add_f32_e32 v58, v59, v61
	v_mov_b32_e32 v57, v56
	s_nop 1
	v_permlane32_swap_b32_e32 v57, v56
	v_mov_b32_e32 v59, v58
	s_nop 1
	v_permlane32_swap_b32_e32 v59, v58
	s_and_saveexec_b64 s[30:31], s[0:1]
	s_cbranch_execz .LBB0_1693
	v_pk_add_f32 v[46:47], v[44:45], v[46:47]
	v_add_f32_e32 v48, v48, v49
	v_cmp_gt_f32_e32 vcc, v47, v46
	v_add_f32_e32 v50, v50, v51
	v_add_f32_e32 v52, v52, v53
	v_cndmask_b32_e32 v44, v46, v47, vcc
	v_cmp_gt_f32_e64 s[2:3], v48, v44
	s_waitcnt lgkmcnt(2)
	v_add_f32_e32 v54, v54, v55
	s_waitcnt lgkmcnt(1)
	v_add_f32_e32 v56, v56, v57
	v_cndmask_b32_e64 v44, v44, v48, s[2:3]
	v_cmp_gt_f32_e64 s[4:5], v50, v44
	s_waitcnt lgkmcnt(0)
	v_add_f32_e32 v58, v58, v59
	v_cmp_nlg_f32_e64 s[14:15], s43, v46
	v_cndmask_b32_e64 v44, v44, v50, s[4:5]
	v_cmp_gt_f32_e64 s[6:7], v52, v44
	s_ashr_i32 s21, s20, 31
	s_nop 0
	v_cndmask_b32_e64 v44, v44, v52, s[6:7]
	v_cmp_gt_f32_e64 s[8:9], v54, v44
	s_nop 1
	v_cndmask_b32_e64 v44, v44, v54, s[8:9]
	v_cmp_gt_f32_e64 s[10:11], v56, v44
	s_nop 1
	v_cndmask_b32_e64 v49, v44, v56, s[10:11]
	v_cndmask_b32_e64 v44, 0, 1, vcc
	v_cndmask_b32_e64 v44, v44, 2, s[2:3]
	v_cndmask_b32_e64 v44, v44, 3, s[4:5]
	v_cndmask_b32_e64 v44, v44, 4, s[6:7]
	v_cndmask_b32_e64 v44, v44, 5, s[8:9]
	v_cndmask_b32_e64 v44, v44, 6, s[10:11]
	v_cmp_ngt_f32_e32 vcc, v58, v49
	s_and_b64 s[46:47], s[10:11], vcc
	s_nop 0
	v_cndmask_b32_e32 v44, 7, v44, vcc
	v_cmp_eq_u32_e64 s[12:13], 0, v44
	s_or_b64 s[12:13], s[12:13], s[14:15]
	v_cmp_ne_u32_e64 s[10:11], 1, v44
	v_cndmask_b32_e64 v45, v46, v92, s[12:13]
	v_cmp_gt_f32_e64 s[12:13], v47, v45
	s_and_b64 s[10:11], s[10:11], s[12:13]
	v_cndmask_b32_e64 v45, v45, v47, s[10:11]
	v_cmp_ne_u32_e64 s[8:9], 2, v44
	v_cmp_gt_f32_e64 s[12:13], v48, v45
	s_and_b64 s[8:9], s[8:9], s[12:13]
	v_cndmask_b32_e64 v45, v45, v48, s[8:9]
	v_cmp_ne_u32_e64 s[6:7], 3, v44
	v_cmp_gt_f32_e64 s[12:13], v50, v45
	s_and_b64 s[6:7], s[6:7], s[12:13]
	v_cndmask_b32_e64 v45, v45, v50, s[6:7]
	v_cmp_ne_u32_e64 s[4:5], 4, v44
	v_cmp_gt_f32_e64 s[12:13], v52, v45
	s_and_b64 s[4:5], s[4:5], s[12:13]
	v_cndmask_b32_e64 v45, v45, v52, s[4:5]
	v_cmp_ne_u32_e64 s[2:3], 5, v44
	v_cmp_gt_f32_e64 s[12:13], v54, v45
	s_and_b64 s[2:3], s[2:3], s[12:13]
	v_cndmask_b32_e64 v45, v45, v54, s[2:3]
	v_cmp_ngt_f32_e64 s[12:13], v56, v45
	s_or_b64 s[12:13], s[46:47], s[12:13]
	v_cndmask_b32_e32 v47, v58, v49, vcc
	v_cndmask_b32_e64 v46, v56, v45, s[12:13]
	v_cndmask_b32_e64 v45, 0, 1, s[10:11]
	v_cndmask_b32_e64 v45, v45, 2, s[8:9]
	v_cndmask_b32_e64 v45, v45, 3, s[6:7]
	v_cmp_gt_f32_e64 s[14:15], v58, v46
	v_cndmask_b32_e64 v45, v45, 4, s[4:5]
	v_cndmask_b32_e64 v45, v45, 5, s[2:3]
	s_and_b64 s[2:3], vcc, s[14:15]
	v_cndmask_b32_e64 v46, v46, v58, s[2:3]
	v_sub_f32_e32 v46, v47, v46
	v_mul_f32_e32 v46, 0x3fb8aa3b, v46
	v_exp_f32_e32 v46, v46
	v_cndmask_b32_e64 v45, 6, v45, s[12:13]
	v_cndmask_b32_e64 v45, v45, 7, s[2:3]
	v_add_f32_e32 v46, 1.0, v46
	v_div_scale_f32 v47, s[2:3], v46, v46, 1.0
	v_rcp_f32_e32 v48, v47
	s_lshl_b64 s[2:3], s[20:21], 2
	s_add_u32 s4, s35, s2
	s_addc_u32 s5, s36, s3
	v_fma_f32 v49, -v47, v48, 1.0
	v_fmac_f32_e32 v48, v49, v48
	v_div_scale_f32 v49, vcc, 1.0, v46, 1.0
	v_mul_f32_e32 v50, v49, v48
	v_fma_f32 v51, -v47, v50, v49
	v_fmac_f32_e32 v50, v51, v48
	v_fma_f32 v47, -v47, v50, v49
	v_div_fmas_f32 v47, v47, v48, v50
	s_add_i32 s6, s20, 1
	v_div_fixup_f32 v48, v47, v46, 1.0
	v_lshl_add_u32 v46, v44, 2, s44
	s_ashr_i32 s7, s6, 31
	ds_add_rtn_u32 v46, v46, v93
	v_lshl_add_u32 v47, v45, 2, s44
	s_add_u32 s2, s37, s2
	v_sub_f32_e32 v49, 1.0, v48
	ds_add_rtn_u32 v47, v47, v93
	s_addc_u32 s3, s38, s3
	global_store_dword v91, v49, s[2:3]
	s_lshl_b64 s[2:3], s[6:7], 2
	s_add_u32 s2, s37, s2
	s_addc_u32 s3, s38, s3
	global_store_dword v91, v48, s[2:3]
	v_mov_b32_e32 v48, s19
	global_store_dwordx2 v91, v[44:45], s[4:5]
	s_waitcnt lgkmcnt(0)
	ds_write_b128 v48, v[44:47]
	s_branch .LBB0_1693
